# v15 + nt on the P7 residual x loads and the P1 LN1 x loads (far-reuse input stream)
# speedup vs baseline: 1.0474x; 1.0253x over previous
.LBB0_135:
	global_load_dwordx4 v[14:17], v[44:45], off offset:-4096 nt
	global_load_dwordx4 v[10:13], v[44:45], off offset:-3072 nt
	global_load_dwordx4 v[18:21], v[44:45], off offset:-2048 nt
	global_load_dwordx4 v[22:25], v[44:45], off nt
	global_load_dwordx4 v[26:29], v[44:45], off offset:-1024 nt
	global_load_dwordx4 v[30:33], v[44:45], off offset:1024 nt
	global_load_dwordx4 v[34:37], v[44:45], off offset:3072 nt
	global_load_dwordx4 v[38:41], v[44:45], off offset:2048 nt
	v_mov_b32_e32 v135, 0
	ds_read_b128 v[56:59], v51 offset:1024
	ds_read_b128 v[60:63], v51 offset:2048
	ds_read_b128 v[64:67], v51 offset:10240
	ds_read_b128 v[68:71], v51 offset:11264
	ds_read_b128 v[72:75], v51 offset:3072
	ds_read_b128 v[76:79], v51 offset:4096
	ds_read_b128 v[80:83], v51 offset:12288
	ds_read_b128 v[84:87], v51 offset:13312
	ds_read_b128 v[88:91], v51 offset:5120
	ds_read_b128 v[92:95], v51 offset:6144
	ds_read_b128 v[96:99], v51 offset:9216
	ds_read_b128 v[100:103], v51 offset:7168
	ds_read_b128 v[104:107], v51 offset:14336
	ds_read_b128 v[108:111], v51 offset:15360
	v_mov_b32_e32 v55, 0
	v_mov_b32_e32 v138, 0
	v_mov_b32_e32 v139, 0
	v_mov_b32_e32 v140, 0
	v_mov_b32_e32 v141, 0
	v_mov_b32_e32 v142, 0
	v_mov_b32_e32 v143, 0
	s_add_i32 s4, s4, s6
	v_lshl_add_u64 v[44:45], v[44:45], 0, s[10:11]
	s_cmpk_gt_i32 s4, 0x1fff
	s_waitcnt vmcnt(7)
	v_mov_b32_e32 v114, v15
	s_waitcnt vmcnt(6)
	v_mov_b32_e32 v115, v11
	v_mov_b32_e32 v118, v17
	v_mov_b32_e32 v119, v13
	v_mov_b32_e32 v112, v14
	v_mov_b32_e32 v113, v10
	v_mov_b32_e32 v116, v16
	v_mov_b32_e32 v117, v12
	s_waitcnt vmcnt(5)
	v_pk_mul_f32 v[120:121], v[20:21], v[20:21]
	v_pk_mul_f32 v[122:123], v[18:19], v[18:19]
	v_pk_mul_f32 v[114:115], v[114:115], v[114:115]
	v_pk_mul_f32 v[118:119], v[118:119], v[118:119]
	v_pk_mov_b32 v[136:137], v[122:123], v[120:121] op_sel:[1,0]
	v_mov_b32_e32 v123, v121
	v_pk_fma_f32 v[112:113], v[112:113], v[112:113], v[114:115]
	v_pk_fma_f32 v[114:115], v[116:117], v[116:117], v[118:119]
	s_waitcnt vmcnt(3)
	v_mul_f32_e32 v124, v27, v27
	v_mul_f32_e32 v126, v29, v29
	v_pk_add_f32 v[116:117], v[136:137], v[122:123]
	v_pk_add_f32 v[112:113], v[112:113], v[114:115]
	v_mul_f32_e32 v144, v22, v22
	v_mul_f32_e32 v145, v23, v23
	v_mul_f32_e32 v146, v24, v24
	v_mul_f32_e32 v147, v25, v25
	v_pk_fma_f32 v[120:121], v[26:27], v[26:27], v[124:125] op_sel_hi:[1,1,0]
	v_pk_fma_f32 v[124:125], v[28:29], v[28:29], v[126:127] op_sel_hi:[1,1,0]
	v_pk_add_f32 v[114:115], v[116:117], v[116:117] op_sel:[0,1] op_sel_hi:[1,0]
	v_pk_add_f32 v[112:113], v[112:113], v[112:113] op_sel:[0,1] op_sel_hi:[1,0]
	s_waitcnt vmcnt(2)
	v_pk_mul_f32 v[128:129], v[32:33], v[32:33]
	v_pk_mul_f32 v[130:131], v[30:31], v[30:31]
	v_mov_b32_e32 v121, v146
	v_mov_b32_e32 v125, v147
	v_mov_b32_e32 v115, v145
	v_mov_b32_e32 v113, v144
	v_pk_mov_b32 v[126:127], v[130:131], v[128:129] op_sel:[1,0]
	v_mov_b32_e32 v131, v129
	v_pk_add_f32 v[116:117], v[120:121], v[124:125]
	v_pk_add_f32 v[112:113], v[112:113], v[114:115]
	s_waitcnt vmcnt(0)
	v_mul_f32_e32 v132, v39, v39
	v_mul_f32_e32 v134, v41, v41
	v_pk_add_f32 v[118:119], v[126:127], v[130:131]
	v_pk_add_f32 v[112:113], v[112:113], v[116:117]
	v_mul_f32_e32 v148, v34, v34
	v_mul_f32_e32 v149, v35, v35
	v_mul_f32_e32 v150, v36, v36
	v_mul_f32_e32 v151, v37, v37
	v_pk_fma_f32 v[128:129], v[38:39], v[38:39], v[132:133] op_sel_hi:[1,1,0]
	v_pk_fma_f32 v[132:133], v[40:41], v[40:41], v[134:135] op_sel_hi:[1,1,0]
	v_pk_add_f32 v[118:119], v[118:119], v[118:119] op_sel:[0,1] op_sel_hi:[1,0]
	v_pk_add_f32 v[112:113], v[112:113], v[112:113] op_sel:[0,1] op_sel_hi:[1,0]
	v_mov_b32_e32 v129, v150
	v_mov_b32_e32 v133, v151
	v_mov_b32_e32 v119, v149
	v_mov_b32_e32 v113, v148
	v_pk_add_f32 v[120:121], v[128:129], v[132:133]
	v_pk_add_f32 v[112:113], v[112:113], v[118:119]
	s_nop 0
	v_pk_add_f32 v[112:113], v[112:113], v[120:121]
	s_nop 0
	v_add_f32_e32 v112, v112, v113
	ds_bpermute_b32 v113, v1, v112
	s_waitcnt lgkmcnt(0)
	v_add_f32_e32 v112, v112, v113
	ds_bpermute_b32 v113, v46, v112
	s_waitcnt lgkmcnt(0)
	v_add_f32_e32 v112, v112, v113
	ds_bpermute_b32 v113, v47, v112
	s_waitcnt lgkmcnt(0)
	v_add_f32_e32 v112, v112, v113
	ds_bpermute_b32 v113, v48, v112
	s_waitcnt lgkmcnt(0)
	v_add_f32_e32 v112, v112, v113
	ds_bpermute_b32 v113, v49, v112
	s_waitcnt lgkmcnt(0)
	v_add_f32_e32 v112, v112, v113
	ds_bpermute_b32 v113, v50, v112
	s_waitcnt lgkmcnt(0)
	v_add_f32_e32 v112, v112, v113
	v_fmamk_f32 v112, v112, 0x3a000000, v52
	v_mul_f32_e32 v113, 0x4f800000, v112
	v_cmp_gt_f32_e32 vcc, s5, v112
	s_nop 1
	v_cndmask_b32_e32 v112, v112, v113, vcc
	v_sqrt_f32_e32 v113, v112
	s_nop 0
	v_add_u32_e32 v114, -1, v113
	v_add_u32_e32 v115, 1, v113
	v_fma_f32 v116, -v114, v113, v112
	v_fma_f32 v117, -v115, v113, v112
	v_cmp_ge_f32_e64 s[0:1], 0, v116
	s_nop 1
	v_cndmask_b32_e64 v113, v113, v114, s[0:1]
	v_cmp_lt_f32_e64 s[0:1], 0, v117
	s_nop 1
	v_cndmask_b32_e64 v113, v113, v115, s[0:1]
	v_mul_f32_e32 v114, 0x37800000, v113
	v_cndmask_b32_e32 v113, v113, v114, vcc
	v_cmp_class_f32_e32 vcc, v112, v53
	s_nop 1
	v_cndmask_b32_e32 v112, v113, v112, vcc
	v_div_scale_f32 v113, s[0:1], v112, v112, 1.0
	v_rcp_f32_e32 v115, v113
	v_div_scale_f32 v114, vcc, 1.0, v112, 1.0
	v_fma_f32 v116, -v113, v115, 1.0
	v_fmac_f32_e32 v115, v116, v115
	v_mul_f32_e32 v116, v114, v115
	v_fma_f32 v117, -v113, v116, v114
	v_fmac_f32_e32 v116, v117, v115
	v_fma_f32 v113, -v113, v116, v114
	v_div_fmas_f32 v113, v113, v115, v116
	v_div_fixup_f32 v112, v113, v112, 1.0
	v_pk_mul_f32 v[14:15], v[14:15], v[112:113] op_sel_hi:[1,0]
	v_pk_mul_f32 v[10:11], v[10:11], v[112:113] op_sel_hi:[1,0]
	v_pk_fma_f32 v[14:15], v[2:3], v[14:15], v[6:7]
	v_pk_mul_f32 v[18:19], v[18:19], v[112:113] op_sel_hi:[1,0]
	v_pk_fma_f32 v[10:11], v[56:57], v[10:11], v[96:97]
	v_med3_f32 v14, v14, s7, v54
	v_med3_f32 v15, v15, s7, v54
	v_pk_mul_f32 v[26:27], v[26:27], v[112:113] op_sel_hi:[1,0]
	v_pk_fma_f32 v[18:19], v[18:19], v[60:61], v[64:65]
	v_med3_f32 v10, v10, s7, v54
	v_med3_f32 v11, v11, s7, v54
	v_cvt_pk_fp8_f32 v55, v14, v15
	v_pk_mul_f32 v[16:17], v[16:17], v[112:113] op_sel_hi:[1,0]
	v_pk_mul_f32 v[22:23], v[22:23], v[112:113] op_sel_hi:[1,0]
	v_pk_mul_f32 v[30:31], v[30:31], v[112:113] op_sel_hi:[1,0]
	v_pk_mul_f32 v[38:39], v[38:39], v[112:113] op_sel_hi:[1,0]
	v_pk_mul_f32 v[34:35], v[34:35], v[112:113] op_sel_hi:[1,0]
	v_pk_fma_f32 v[26:27], v[26:27], v[72:73], v[68:69]
	v_med3_f32 v18, v18, s7, v54
	v_med3_f32 v19, v19, s7, v54
	v_cvt_pk_fp8_f32 v135, v10, v11
	v_pk_mul_f32 v[12:13], v[12:13], v[112:113] op_sel_hi:[1,0]
	v_pk_fma_f32 v[16:17], v[4:5], v[16:17], v[8:9]
	v_pk_fma_f32 v[22:23], v[22:23], v[76:77], v[80:81]
	v_pk_fma_f32 v[30:31], v[30:31], v[88:89], v[84:85]
	v_pk_fma_f32 v[38:39], v[38:39], v[92:93], v[104:105]
	v_pk_fma_f32 v[34:35], v[34:35], v[100:101], v[108:109]
	v_med3_f32 v26, v26, s7, v54
	v_med3_f32 v27, v27, s7, v54
	v_cvt_pk_fp8_f32 v138, v18, v19
	v_pk_mul_f32 v[20:21], v[20:21], v[112:113] op_sel_hi:[1,0]
	v_pk_fma_f32 v[12:13], v[58:59], v[12:13], v[98:99]
	v_med3_f32 v16, v16, s7, v54
	v_med3_f32 v17, v17, s7, v54
	v_med3_f32 v22, v22, s7, v54
	v_med3_f32 v23, v23, s7, v54
	v_med3_f32 v30, v30, s7, v54
	v_med3_f32 v31, v31, s7, v54
	v_med3_f32 v38, v38, s7, v54
	v_med3_f32 v39, v39, s7, v54
	v_med3_f32 v34, v34, s7, v54
	v_med3_f32 v35, v35, s7, v54
	v_cvt_pk_fp8_f32 v139, v26, v27
	v_pk_mul_f32 v[28:29], v[28:29], v[112:113] op_sel_hi:[1,0]
	v_pk_fma_f32 v[20:21], v[20:21], v[62:63], v[66:67]
	v_med3_f32 v12, v12, s7, v54
	v_med3_f32 v13, v13, s7, v54
	v_cvt_pk_fp8_f32 v140, v22, v23
	v_cvt_pk_fp8_f32 v141, v30, v31
	v_cvt_pk_fp8_f32 v142, v38, v39
	v_cvt_pk_fp8_f32 v143, v34, v35
	v_cvt_pk_fp8_f32 v55, v16, v17 op_sel:[0,0,1]
	v_pk_mul_f32 v[24:25], v[24:25], v[112:113] op_sel_hi:[1,0]
	v_pk_mul_f32 v[32:33], v[32:33], v[112:113] op_sel_hi:[1,0]
	v_pk_mul_f32 v[40:41], v[40:41], v[112:113] op_sel_hi:[1,0]
	v_pk_mul_f32 v[36:37], v[36:37], v[112:113] op_sel_hi:[1,0]
	v_pk_fma_f32 v[28:29], v[28:29], v[74:75], v[70:71]
	v_med3_f32 v20, v20, s7, v54
	v_med3_f32 v21, v21, s7, v54
	v_cvt_pk_fp8_f32 v135, v12, v13 op_sel:[0,0,1]
	v_pk_fma_f32 v[24:25], v[24:25], v[78:79], v[82:83]
	v_pk_fma_f32 v[32:33], v[32:33], v[90:91], v[86:87]
	v_pk_fma_f32 v[40:41], v[40:41], v[94:95], v[106:107]
	v_pk_fma_f32 v[36:37], v[36:37], v[102:103], v[110:111]
	v_med3_f32 v28, v28, s7, v54
	v_med3_f32 v29, v29, s7, v54
	v_cvt_pk_fp8_f32 v138, v20, v21 op_sel:[0,0,1]
	v_med3_f32 v24, v24, s7, v54
	v_med3_f32 v25, v25, s7, v54
	v_med3_f32 v32, v32, s7, v54
	v_med3_f32 v33, v33, s7, v54
	v_med3_f32 v40, v40, s7, v54
	v_med3_f32 v41, v41, s7, v54
	v_med3_f32 v36, v36, s7, v54
	v_med3_f32 v37, v37, s7, v54
	v_cvt_pk_fp8_f32 v139, v28, v29 op_sel:[0,0,1]
	v_cvt_pk_fp8_f32 v140, v24, v25 op_sel:[0,0,1]
	v_cvt_pk_fp8_f32 v141, v32, v33 op_sel:[0,0,1]
	v_cvt_pk_fp8_f32 v142, v40, v41 op_sel:[0,0,1]
	v_cvt_pk_fp8_f32 v143, v36, v37 op_sel:[0,0,1]
	global_store_dword v[42:43], v55, off
	global_store_dword v[42:43], v135, off offset:256
	global_store_dword v[42:43], v138, off offset:512
	global_store_dword v[42:43], v139, off offset:768
	global_store_dword v[42:43], v140, off offset:1024
	global_store_dword v[42:43], v141, off offset:1280
	global_store_dword v[42:43], v142, off offset:1536
	global_store_dword v[42:43], v143, off offset:1792
	v_lshl_add_u64 v[42:43], v[42:43], 0, s[8:9]
	s_cbranch_scc0 .LBB0_135

.LBB0_1150:
	v_lshl_or_b32 v6, s71, 8, v202
	v_ashrrev_i32_e32 v7, 31, v6
	v_add_u32_e32 v10, s70, v200
	v_lshl_add_u64 v[8:9], v[6:7], 2, s[14:15]
	v_ashrrev_i32_e32 v11, 31, v10
	global_load_dwordx4 v[16:19], v[8:9], off
	global_load_dwordx4 v[20:23], v[8:9], off offset:64
	global_load_dwordx4 v[24:27], v[8:9], off offset:512
	global_load_dwordx4 v[28:31], v[8:9], off offset:576
	v_lshlrev_b64 v[10:11], 11, v[10:11]
	v_lshl_add_u64 v[6:7], v[10:11], 0, v[6:7]
	v_lshlrev_b32_e32 v14, 2, v6
	global_load_dwordx4 v[212:215], v14, s[6:7] nt
	global_load_dwordx4 v[216:219], v14, s[6:7] offset:64 nt
	global_load_dwordx4 v[220:223], v14, s[6:7] offset:512 nt
	global_load_dwordx4 v[224:227], v14, s[6:7] offset:576 nt
	v_add_u32_e32 v12, s24, v14
	global_load_dwordx4 v[228:231], v12, s[6:7] nt
	global_load_dwordx4 v[232:235], v12, s[6:7] offset:64 nt
	global_load_dwordx4 v[236:239], v12, s[6:7] offset:512 nt
	global_load_dwordx4 v[240:243], v12, s[6:7] offset:576 nt
	v_add_u32_e32 v12, s10, v14
	global_load_dwordx4 v[244:247], v12, s[6:7] nt
	global_load_dwordx4 v[248:251], v12, s[6:7] offset:64 nt
	global_load_dwordx4 v[2:5], v12, s[6:7] offset:512 nt
	global_load_dwordx4 v[8:11], v12, s[6:7] offset:576 nt
	s_andn2_b64 vcc, exec, s[0:1]
	s_mov_b64 s[0:1], -1
	s_nop 15
	s_waitcnt vmcnt(12)
	v_pk_mul_f32 v[16:17], v[16:17], s[22:23] op_sel_hi:[1,0]
	v_pk_mul_f32 v[18:19], v[18:19], s[22:23] op_sel_hi:[1,0]
	v_pk_mul_f32 v[20:21], v[20:21], s[22:23] op_sel_hi:[1,0]
	v_pk_mul_f32 v[22:23], v[22:23], s[22:23] op_sel_hi:[1,0]
	v_pk_mul_f32 v[24:25], v[24:25], s[22:23] op_sel_hi:[1,0]
	v_pk_mul_f32 v[26:27], v[26:27], s[22:23] op_sel_hi:[1,0]
	v_pk_mul_f32 v[28:29], v[28:29], s[22:23] op_sel_hi:[1,0]
	v_pk_mul_f32 v[30:31], v[30:31], s[22:23] op_sel_hi:[1,0]
	s_waitcnt vmcnt(8)
	v_pk_fma_f32 v[214:215], v[160:161], v[18:19], v[214:215]
	v_pk_fma_f32 v[212:213], v[158:159], v[16:17], v[212:213]
	v_pk_fma_f32 v[218:219], v[156:157], v[22:23], v[218:219]
	v_pk_fma_f32 v[216:217], v[154:155], v[20:21], v[216:217]
	v_pk_fma_f32 v[222:223], v[152:153], v[26:27], v[222:223]
	v_pk_fma_f32 v[220:221], v[150:151], v[24:25], v[220:221]
	v_pk_fma_f32 v[226:227], v[140:141], v[30:31], v[226:227]
	v_pk_fma_f32 v[224:225], v[138:139], v[28:29], v[224:225]
	global_store_dwordx4 v14, v[212:215], s[48:49]
	global_store_dwordx4 v14, v[216:219], s[48:49] offset:64
	global_store_dwordx4 v14, v[220:223], s[48:49] offset:512
	global_store_dwordx4 v14, v[224:227], s[48:49] offset:576
	v_add_u32_e32 v12, s26, v14
	global_load_dwordx4 v[212:215], v12, s[6:7] nt
	global_load_dwordx4 v[216:219], v12, s[6:7] offset:64 nt
	global_load_dwordx4 v[220:223], v12, s[6:7] offset:512 nt
	global_load_dwordx4 v[224:227], v12, s[6:7] offset:576 nt
	s_waitcnt vmcnt(8)
	v_pk_fma_f32 v[230:231], v[148:149], v[18:19], v[230:231]
	v_pk_fma_f32 v[228:229], v[146:147], v[16:17], v[228:229]
	v_pk_fma_f32 v[234:235], v[144:145], v[22:23], v[234:235]
	v_pk_fma_f32 v[232:233], v[142:143], v[20:21], v[232:233]
	v_pk_fma_f32 v[238:239], v[136:137], v[26:27], v[238:239]
	v_pk_fma_f32 v[236:237], v[134:135], v[24:25], v[236:237]
	v_pk_fma_f32 v[242:243], v[124:125], v[30:31], v[242:243]
	v_pk_fma_f32 v[240:241], v[122:123], v[28:29], v[240:241]
	v_add_u32_e32 v13, s24, v14
	global_store_dwordx4 v13, v[228:231], s[48:49]
	global_store_dwordx4 v13, v[232:235], s[48:49] offset:64
	global_store_dwordx4 v13, v[236:239], s[48:49] offset:512
	global_store_dwordx4 v13, v[240:243], s[48:49] offset:576
	v_add_u32_e32 v12, s28, v14
	global_load_dwordx4 v[228:231], v12, s[6:7] nt
	global_load_dwordx4 v[232:235], v12, s[6:7] offset:64 nt
	global_load_dwordx4 v[236:239], v12, s[6:7] offset:512 nt
	global_load_dwordx4 v[240:243], v12, s[6:7] offset:576 nt
	s_waitcnt vmcnt(8)
	v_pk_fma_f32 v[246:247], v[132:133], v[18:19], v[246:247]
	v_pk_fma_f32 v[244:245], v[130:131], v[16:17], v[244:245]
	v_pk_fma_f32 v[250:251], v[128:129], v[22:23], v[250:251]
	v_pk_fma_f32 v[248:249], v[126:127], v[20:21], v[248:249]
	v_pk_fma_f32 v[4:5], v[120:121], v[26:27], v[4:5]
	v_pk_fma_f32 v[2:3], v[118:119], v[24:25], v[2:3]
	v_pk_fma_f32 v[10:11], v[108:109], v[30:31], v[10:11]
	v_pk_fma_f32 v[8:9], v[106:107], v[28:29], v[8:9]
	v_add_u32_e32 v13, s10, v14
	global_store_dwordx4 v13, v[244:247], s[48:49]
	global_store_dwordx4 v13, v[248:251], s[48:49] offset:64
	global_store_dwordx4 v13, v[2:5], s[48:49] offset:512
	global_store_dwordx4 v13, v[8:11], s[48:49] offset:576
	v_add_u32_e32 v12, s30, v14
	global_load_dwordx4 v[244:247], v12, s[6:7] nt
	global_load_dwordx4 v[248:251], v12, s[6:7] offset:64 nt
	global_load_dwordx4 v[2:5], v12, s[6:7] offset:512 nt
	global_load_dwordx4 v[8:11], v12, s[6:7] offset:576 nt
	s_waitcnt vmcnt(8)
	v_pk_fma_f32 v[214:215], v[116:117], v[18:19], v[214:215]
	v_pk_fma_f32 v[212:213], v[114:115], v[16:17], v[212:213]
	v_pk_fma_f32 v[218:219], v[112:113], v[22:23], v[218:219]
	v_pk_fma_f32 v[216:217], v[110:111], v[20:21], v[216:217]
	v_pk_fma_f32 v[222:223], v[104:105], v[26:27], v[222:223]
	v_pk_fma_f32 v[220:221], v[102:103], v[24:25], v[220:221]
	v_pk_fma_f32 v[226:227], v[100:101], v[30:31], v[226:227]
	v_pk_fma_f32 v[224:225], v[98:99], v[28:29], v[224:225]
	v_add_u32_e32 v13, s26, v14
	global_store_dwordx4 v13, v[212:215], s[48:49]
	global_store_dwordx4 v13, v[216:219], s[48:49] offset:64
	global_store_dwordx4 v13, v[220:223], s[48:49] offset:512
	global_store_dwordx4 v13, v[224:227], s[48:49] offset:576
	v_add_u32_e32 v12, s34, v14
	global_load_dwordx4 v[212:215], v12, s[6:7] nt
	global_load_dwordx4 v[216:219], v12, s[6:7] offset:64 nt
	global_load_dwordx4 v[220:223], v12, s[6:7] offset:512 nt
	global_load_dwordx4 v[224:227], v12, s[6:7] offset:576 nt
	s_waitcnt vmcnt(8)
	v_pk_fma_f32 v[230:231], v[96:97], v[18:19], v[230:231]
	v_pk_fma_f32 v[228:229], v[94:95], v[16:17], v[228:229]
	v_pk_fma_f32 v[234:235], v[92:93], v[22:23], v[234:235]
	v_pk_fma_f32 v[232:233], v[90:91], v[20:21], v[232:233]
	v_pk_fma_f32 v[238:239], v[88:89], v[26:27], v[238:239]
	v_pk_fma_f32 v[236:237], v[86:87], v[24:25], v[236:237]
	v_pk_fma_f32 v[242:243], v[76:77], v[30:31], v[242:243]
	v_pk_fma_f32 v[240:241], v[74:75], v[28:29], v[240:241]
	v_add_u32_e32 v13, s28, v14
	global_store_dwordx4 v13, v[228:231], s[48:49]
	global_store_dwordx4 v13, v[232:235], s[48:49] offset:64
	global_store_dwordx4 v13, v[236:239], s[48:49] offset:512
	global_store_dwordx4 v13, v[240:243], s[48:49] offset:576
	v_add_u32_e32 v12, s36, v14
	global_load_dwordx4 v[228:231], v12, s[6:7] nt
	global_load_dwordx4 v[232:235], v12, s[6:7] offset:64 nt
	global_load_dwordx4 v[236:239], v12, s[6:7] offset:512 nt
	global_load_dwordx4 v[240:243], v12, s[6:7] offset:576 nt
	s_waitcnt vmcnt(8)
	v_pk_fma_f32 v[246:247], v[84:85], v[18:19], v[246:247]
	v_pk_fma_f32 v[244:245], v[82:83], v[16:17], v[244:245]
	v_pk_fma_f32 v[250:251], v[80:81], v[22:23], v[250:251]
	v_pk_fma_f32 v[248:249], v[78:79], v[20:21], v[248:249]
	v_pk_fma_f32 v[4:5], v[72:73], v[26:27], v[4:5]
	v_pk_fma_f32 v[2:3], v[70:71], v[24:25], v[2:3]
	v_pk_fma_f32 v[10:11], v[60:61], v[30:31], v[10:11]
	v_pk_fma_f32 v[8:9], v[58:59], v[28:29], v[8:9]
	v_add_u32_e32 v13, s30, v14
	global_store_dwordx4 v13, v[244:247], s[48:49]
	global_store_dwordx4 v13, v[248:251], s[48:49] offset:64
	global_store_dwordx4 v13, v[2:5], s[48:49] offset:512
	global_store_dwordx4 v13, v[8:11], s[48:49] offset:576
	s_waitcnt vmcnt(4)
	v_pk_fma_f32 v[214:215], v[68:69], v[18:19], v[214:215]
	v_pk_fma_f32 v[212:213], v[66:67], v[16:17], v[212:213]
	v_pk_fma_f32 v[218:219], v[64:65], v[22:23], v[218:219]
	v_pk_fma_f32 v[216:217], v[62:63], v[20:21], v[216:217]
	v_pk_fma_f32 v[222:223], v[56:57], v[26:27], v[222:223]
	v_pk_fma_f32 v[220:221], v[54:55], v[24:25], v[220:221]
	v_pk_fma_f32 v[226:227], v[44:45], v[30:31], v[226:227]
	v_pk_fma_f32 v[224:225], v[42:43], v[28:29], v[224:225]
	v_add_u32_e32 v13, s34, v14
	global_store_dwordx4 v13, v[212:215], s[48:49]
	global_store_dwordx4 v13, v[216:219], s[48:49] offset:64
	global_store_dwordx4 v13, v[220:223], s[48:49] offset:512
	global_store_dwordx4 v13, v[224:227], s[48:49] offset:576
	s_waitcnt vmcnt(0)
	v_pk_fma_f32 v[230:231], v[52:53], v[18:19], v[230:231]
	v_pk_fma_f32 v[228:229], v[50:51], v[16:17], v[228:229]
	v_pk_fma_f32 v[234:235], v[48:49], v[22:23], v[234:235]
	v_pk_fma_f32 v[232:233], v[46:47], v[20:21], v[232:233]
	v_pk_fma_f32 v[238:239], v[40:41], v[26:27], v[238:239]
	v_pk_fma_f32 v[236:237], v[38:39], v[24:25], v[236:237]
	v_pk_fma_f32 v[242:243], v[36:37], v[30:31], v[242:243]
	v_pk_fma_f32 v[240:241], v[34:35], v[28:29], v[240:241]
	v_add_u32_e32 v13, s36, v14
	global_store_dwordx4 v13, v[228:231], s[48:49]
	global_store_dwordx4 v13, v[232:235], s[48:49] offset:64
	global_store_dwordx4 v13, v[236:239], s[48:49] offset:512
	global_store_dwordx4 v13, v[240:243], s[48:49] offset:576
	s_cbranch_vccnz .LBB0_1134
	s_andn2_b64 vcc, exec, s[12:13]
	s_cbranch_vccnz .LBB0_1133
	s_barrier
	s_branch .LBB0_1133
